# rwkv_pre S3: waves 0/1 skip the MFMA part (waves 2/3 take two tiles), diagonal-block coefficient and rhs loads use one base register with immediate offsets
# baseline (speedup 1.0000x reference)
.LBB0_625:
	s_cmp_lg_u32 s11, 0
	s_cselect_b64 s[4:5], -1, 0
	s_cmp_eq_u32 s11, 0
	s_cbranch_scc1 .LBB0_629
	v_readfirstlane_b32 s14, v187
	s_lshr_b32 s14, s14, 6
	s_cmp_lt_u32 s14, 2
	s_cbranch_scc1 .LBB0_629
	s_cmp_lt_u32 s14, 4
	s_cbranch_scc1 .Ls3_two
	v_add_u32_e32 v22, 0, v170
	v_add_u32_e32 v18, 0x1b000, v22
	ds_read_b128 v[18:21], v18
	ds_read_b128 v[24:27], v166
	s_cmpk_lg_i32 s11, 0x30c0
	s_waitcnt lgkmcnt(0)
	v_mfma_f32_16x16x32_bf16 v[18:21], v[18:21], v[24:27], 0
	s_cbranch_scc1 .LBB0_628
	v_add_u32_e32 v22, 0x1b040, v22
	ds_read_b128 v[22:25], v22
	ds_read_b128 v[26:29], v166 offset:64
	s_waitcnt lgkmcnt(0)
	v_mfma_f32_16x16x32_bf16 v[18:21], v[22:25], v[26:29], v[18:21]
.LBB0_628:
	s_nop 7
	ds_write2st64_b32 v167, v18, v19 offset1:2
	ds_write2st64_b32 v167, v20, v21 offset0:4 offset1:6
	s_branch .LBB0_629
.Ls3_two:
	v_add_u32_e32 v22, 0, v170
	v_add_u32_e32 v18, 0x1b000, v22
	v_add_u32_e32 v14, 0xffffee00, v166
	ds_read_b128 v[18:21], v18
	ds_read_b128 v[24:27], v166
	ds_read_b128 v[2:5], v14
	v_add_u32_e32 v15, 0xffffff80, v167
	s_cmpk_lg_i32 s11, 0x30c0
	s_cbranch_scc1 .Ls3_two_k1
	v_add_u32_e32 v22, 0x1b040, v22
	ds_read_b128 v[28:31], v22
	ds_read_b128 v[172:175], v166 offset:64
	ds_read_b128 v[176:179], v14 offset:64
	s_waitcnt lgkmcnt(3)
	v_mfma_f32_16x16x32_bf16 v[6:9], v[18:21], v[24:27], 0
	v_mfma_f32_16x16x32_bf16 v[10:13], v[18:21], v[2:5], 0
	s_waitcnt lgkmcnt(0)
	v_mfma_f32_16x16x32_bf16 v[6:9], v[28:31], v[172:175], v[6:9]
	v_mfma_f32_16x16x32_bf16 v[10:13], v[28:31], v[176:179], v[10:13]
	s_branch .Ls3_two_w
.Ls3_two_k1:
	s_waitcnt lgkmcnt(0)
	v_mfma_f32_16x16x32_bf16 v[6:9], v[18:21], v[24:27], 0
	v_mfma_f32_16x16x32_bf16 v[10:13], v[18:21], v[2:5], 0
.Ls3_two_w:
	s_nop 7
	ds_write2st64_b32 v167, v6, v7 offset1:2
	ds_write2st64_b32 v167, v8, v9 offset0:4 offset1:6
	ds_write2st64_b32 v15, v10, v11 offset1:2
	ds_write2st64_b32 v15, v12, v13 offset0:4 offset1:6
.LBB0_629:
	s_and_saveexec_b64 s[12:13], s[0:1]
	s_cbranch_execz .LBB0_635
	s_and_saveexec_b64 s[14:15], s[2:3]
	s_xor_b64 s[14:15], exec, s[14:15]
	s_cbranch_execz .LBB0_632
	v_add_u32_e32 v18, 0x21400, v0
	ds_read_b32 v2, v18
	ds_read_b32 v3, v18 offset:256
	ds_read_b32 v4, v18 offset:512
	ds_read_b32 v5, v18 offset:768
	ds_read_b32 v6, v18 offset:1024
	ds_read_b32 v7, v18 offset:1280
	ds_read_b32 v8, v18 offset:1536
	ds_read_b32 v9, v18 offset:1792
	ds_read_b32 v10, v18 offset:2048
	ds_read_b32 v11, v18 offset:2304
	ds_read_b32 v12, v18 offset:2560
	ds_read_b32 v13, v18 offset:2816
	ds_read_b32 v14, v18 offset:3072
	ds_read_b32 v15, v18 offset:3328
	ds_read_b32 v16, v18 offset:3584
	ds_read_b32 v17, v18 offset:3840

.LBB0_634:
	s_or_b64 exec, exec, s[14:15]
	s_add_i32 s14, s11, 0
	s_add_i32 s15, s14, 0x1d400
	v_mov_b32_e32 v18, s15
	v_add_u32_e32 v19, 0x800, v18
	ds_read_b32 v228, v18 offset:4
	ds_read2_b64 v[70:73], v18 offset0:1 offset1:2
	ds_read2_b64 v[74:77], v18 offset0:33 offset1:34
	ds_read_b32 v230, v18 offset:524
	ds_read_b128 v[78:81], v18 offset:528
	ds_read_b128 v[82:85], v18 offset:784
	ds_read_b32 v233, v18 offset:1044
	ds_read2_b64 v[86:89], v18 offset0:3 offset1:4
	ds_read2_b64 v[90:93], v18 offset0:35 offset1:36
	ds_read2_b64 v[94:97], v18 offset0:131 offset1:132
	ds_read2_b64 v[98:101], v18 offset0:163 offset1:164
	ds_read_b32 v235, v18 offset:1564
	ds_read_b128 v[102:105], v18 offset:544
	ds_read_b128 v[110:113], v18 offset:800
	ds_read_b128 v[118:121], v18 offset:1568
	ds_read_b128 v[122:125], v18 offset:1824
	ds_read_b32 v236, v18 offset:2084
	ds_read2_b64 v[106:109], v18 offset0:5 offset1:6
	ds_read2_b64 v[114:117], v18 offset0:37 offset1:38
	ds_read2_b64 v[126:129], v18 offset0:133 offset1:134
	ds_read2_b64 v[130:133], v18 offset0:165 offset1:166
	ds_read2_b64 v[142:145], v19 offset0:5 offset1:6
	ds_read2_b64 v[146:149], v19 offset0:37 offset1:38
	ds_read_b32 v237, v18 offset:2604
	ds_read_b128 v[134:137], v18 offset:560
	ds_read_b128 v[138:141], v18 offset:816
	ds_read_b128 v[150:153], v18 offset:1584
	ds_read_b128 v[154:157], v18 offset:1840
	ds_read_b128 v[158:161], v18 offset:2608
	ds_read_b128 v[162:165], v18 offset:2864
	ds_read_b32 v238, v18 offset:3124
	ds_read_b64 v[200:201], v18 offset:56
	ds_read_b64 v[202:203], v18 offset:312
	ds_read_b64 v[188:189], v18 offset:1080
	ds_read_b64 v[190:191], v18 offset:1336
	ds_read_b64 v[192:193], v18 offset:2104
	ds_read_b64 v[194:195], v18 offset:2360
	ds_read_b64 v[196:197], v18 offset:3128
	ds_read_b64 v[198:199], v18 offset:3384
	ds_read_b32 v239, v18 offset:3644
